# pre-claim: conversion-pool atomic claims pipelined one item ahead (hide atomic RTT) at all 10 pool sites
# baseline (speedup 1.0000x reference)
.LBB0_27:
	s_or_b64 exec, exec, s[4:5]
	s_waitcnt vmcnt(0)
	v_readfirstlane_b32 s4, v3
	s_nop 1
	v_add_u32_e32 v1, s4, v1
	s_add_i32 s4, 0, 0x20180
	v_mov_b32_e32 v3, s4
	ds_write_b32 v3, v1
	v_cmp_gt_i32_e32 vcc, 0x340, v1
	s_and_saveexec_b64 s[4:5], vcc
	s_cbranch_execz .Lpcp_0
	v_mov_b32_e32 v231, 0
	v_mov_b32_e32 v230, 1
	global_atomic_add v230, v231, v230, s[94:95] offset:256 sc0
.Lpcp_0:
	s_or_b64 exec, exec, s[4:5]
.LBB0_28:
	s_or_b64 exec, exec, s[2:3]
	s_add_u32 s4, s94, 0x9c00000
	s_addc_u32 s5, s95, 0
	s_add_u32 s6, s94, 0x7000000
	s_addc_u32 s7, s95, 0
	s_add_u32 s33, s94, 0x6000000
	s_addc_u32 s52, s95, 0
	s_add_u32 s53, s94, 0x5800000
	s_addc_u32 s54, s95, 0
	s_add_u32 s55, s94, 0x5000000
	s_addc_u32 s56, s95, 0
	s_add_u32 s57, s94, 0x800000
	s_addc_u32 s58, s95, 0
	s_add_i32 s2, 0, 0x20180
	v_mov_b32_e32 v1, s2
	s_waitcnt lgkmcnt(0)
	s_waitcnt lgkmcnt(0)
	s_barrier
	ds_read_b32 v3, v1
	s_movk_i32 s3, 0x33f
	v_lshrrev_b32_e32 v1, 1, v0
	s_movk_i32 s2, 0x340
	v_and_b32_e32 v1, 0xf0, v1
	s_waitcnt lgkmcnt(0)
	v_cmp_lt_i32_e32 vcc, s3, v3
	v_and_b32_e32 v75, 0x7c, v2
	v_readfirstlane_b32 s13, v3
	v_cmp_gt_i32_e64 s[2:3], s2, v3
	s_cbranch_vccnz .LBB0_34
	s_cmpk_gt_i32 s13, 0x67f
	s_cbranch_scc0 .LBB0_35
	s_cmpk_gt_u32 s13, 0x7df
	s_cbranch_scc0 .LBB0_36
	s_cmpk_gt_u32 s13, 0x93f
	s_cbranch_scc0 .LBB0_44
	s_add_i32 s12, s13, 0xfffff6c0
	s_mov_b64 s[10:11], s[82:83]
	s_mov_b32 s27, 1
	s_cbranch_execz .LBB0_45
	s_movk_i32 s14, 0x800
	s_mov_b32 s26, 0
	s_movk_i32 s25, 0x1600
	s_mov_b64 s[68:69], s[4:5]
	s_cbranch_execz .LBB0_37
	s_branch .LBB0_38

.LBB0_71:
	s_cmp_eq_u32 s12, 0
	s_cbranch_scc1 .LBB0_75
	s_waitcnt vmcnt(0)
	v_mov_b32_e32 v66, v230
	s_cmp_eq_u32 s12, 1
	s_cbranch_scc1 .LBB0_76
	v_cmp_gt_i32_e32 vcc, 0x340, v66
	s_and_saveexec_b64 s[28:29], vcc
	s_cbranch_execz .Lpcl_0
	v_mov_b32_e32 v231, 0
	v_mov_b32_e32 v230, 1
	global_atomic_add v230, v231, v230, s[94:95] offset:256 sc0
.Lpcl_0:
	s_or_b64 exec, exec, s[28:29]
	s_branch .LBB0_76

.LBB0_486:
	s_or_b64 exec, exec, s[6:7]
	s_waitcnt vmcnt(0)
	v_readfirstlane_b32 s6, v3
	s_nop 1
	v_add_u32_e32 v2, s6, v2
	s_add_i32 s6, 0, 0x20180
	v_add_u32_e32 v2, 0x680, v2
	v_mov_b32_e32 v3, s6
	ds_write_b32 v3, v2
	v_cmp_gt_i32_e32 vcc, 0x1690, v2
	s_and_saveexec_b64 s[6:7], vcc
	s_cbranch_execz .Lpcp_1
	v_mov_b32_e32 v231, 0
	v_mov_b32_e32 v230, 1
	global_atomic_add v230, v231, v230, s[30:31] offset:1280 sc0
.Lpcp_1:
	s_or_b64 exec, exec, s[6:7]
.LBB0_487:
	s_or_b64 exec, exec, s[2:3]
	s_add_i32 s2, 0, 0x20180
	v_mov_b32_e32 v2, s2
	s_waitcnt lgkmcnt(0)
	s_waitcnt lgkmcnt(0)
	s_barrier
	ds_read_b32 v2, v2
	s_movk_i32 s3, 0x168f
	s_movk_i32 s2, 0x1690
	s_waitcnt lgkmcnt(0)
	v_cmp_lt_i32_e32 vcc, s3, v2
	v_readfirstlane_b32 s12, v2
	v_cmp_gt_i32_e64 s[2:3], s2, v2
	s_cbranch_vccnz .LBB0_493
	s_cmpk_gt_i32 s12, 0x67f
	s_cbranch_scc0 .LBB0_494
	s_cmpk_gt_u32 s12, 0xa9f
	s_cbranch_scc0 .LBB0_495
	s_add_i32 s6, s12, 0xfffff560
	s_bfe_u32 s7, s6, 0x100007
	s_mulk_i32 s7, 0x2493
	s_lshr_b32 s17, s7, 16
	s_mul_i32 s16, s17, 0xfffffc80
	s_add_i32 s16, s16, s6
	s_cmpk_gt_i32 s16, 0x1bf
	s_mul_hi_u32 s19, s17, 0x3800000
	s_mul_i32 s20, s17, 0x3800000
	s_cbranch_scc0 .LBB0_496
	s_cmpk_gt_u32 s16, 0x37f
	s_cbranch_scc0 .LBB0_497
	s_add_i32 s10, s16, 0xfffffc80
	s_add_u32 s6, s26, s20
	s_addc_u32 s7, s27, s19
	s_mul_i32 s11, s17, 0xe00000
	s_add_u32 s11, s30, s11
	s_addc_u32 s13, s31, 0
	s_add_u32 s82, s11, 0x27200000
	s_addc_u32 s83, s13, 0
	s_mov_b64 s[28:29], 0
	s_branch .LBB0_498

.LBB0_549:
	s_cmp_gt_u32 s16, 20
	v_mov_b32_e32 v66, 0x1690
	s_cbranch_scc1 .LBB0_553
	s_waitcnt vmcnt(0)
	v_add_u32_e32 v66, 0x680, v230
	s_cmp_gt_u32 s16, 19
	s_cbranch_scc1 .LBB0_553
	v_cmp_gt_i32_e32 vcc, 0x1690, v66
	s_and_saveexec_b64 s[28:29], vcc
	s_cbranch_execz .Lpcl_1
	v_mov_b32_e32 v231, 0
	v_mov_b32_e32 v230, 1
	v_readlane_b32 s36, v254, 38
	v_readlane_b32 s50, v254, 52
	v_readlane_b32 s51, v254, 53
	v_readlane_b32 s37, v254, 39
	v_readlane_b32 s38, v254, 40
	v_readlane_b32 s39, v254, 41
	v_readlane_b32 s40, v254, 42
	v_readlane_b32 s41, v254, 43
	global_atomic_add v230, v231, v230, s[50:51] offset:1280 sc0
	v_readlane_b32 s42, v254, 44
	v_readlane_b32 s43, v254, 45
	v_readlane_b32 s44, v254, 46
	v_readlane_b32 s45, v254, 47
	v_readlane_b32 s46, v254, 48
	v_readlane_b32 s47, v254, 49
	v_readlane_b32 s48, v254, 50
	v_readlane_b32 s49, v254, 51
.Lpcl_1:
	s_or_b64 exec, exec, s[28:29]
.LBB0_553:
	v_mov_b32_e32 v67, s67
	ds_write_b32 v67, v66

.LBB0_728:
	s_or_b64 exec, exec, s[4:5]
	s_waitcnt vmcnt(0)
	v_readfirstlane_b32 s4, v3
	s_nop 1
	v_add_u32_e32 v2, s4, v2
	s_add_i32 s4, 0, 0x20180
	v_add_u32_e32 v2, 0x680, v2
	v_mov_b32_e32 v3, s4
	ds_write_b32 v3, v2
	v_cmp_gt_i32_e32 vcc, 0x1690, v2
	s_and_saveexec_b64 s[4:5], vcc
	s_cbranch_execz .Lpcp_2
	v_mov_b32_e32 v231, 0
	v_mov_b32_e32 v230, 1
	global_atomic_add v230, v231, v230, s[50:51] offset:1280 sc0
.Lpcp_2:
	s_or_b64 exec, exec, s[4:5]
.LBB0_729:
	s_or_b64 exec, exec, s[2:3]
	s_add_i32 s2, 0, 0x20180
	s_waitcnt vmcnt(15)
	v_mov_b32_e32 v2, s2
	s_waitcnt lgkmcnt(0)
	s_waitcnt lgkmcnt(0)
	s_barrier
	ds_read_b32 v2, v2
	s_movk_i32 s3, 0x168f
	s_movk_i32 s2, 0x1690
	s_waitcnt lgkmcnt(0)
	v_cmp_lt_i32_e32 vcc, s3, v2
	v_readfirstlane_b32 s12, v2
	v_cmp_gt_i32_e64 s[2:3], s2, v2
	s_cbranch_vccnz .LBB0_735
	s_cmpk_gt_i32 s12, 0x67f
	s_cbranch_scc0 .LBB0_736
	s_cmpk_gt_u32 s12, 0xa9f
	s_cbranch_scc0 .LBB0_737
	s_add_i32 s4, s12, 0xfffff560
	s_bfe_u32 s5, s4, 0x100007
	s_mulk_i32 s5, 0x2493
	s_lshr_b32 s19, s5, 16
	s_mul_i32 s17, s19, 0xfffffc80
	s_add_i32 s17, s17, s4
	s_cmpk_gt_i32 s17, 0x1bf
	s_mul_hi_u32 s20, s19, 0x3800000
	s_mul_i32 s21, s19, 0x3800000
	s_cbranch_scc0 .LBB0_738
	s_cmpk_gt_u32 s17, 0x37f
	s_cbranch_scc0 .LBB0_739
	s_add_i32 s10, s17, 0xfffffc80
	s_add_u32 s4, s46, s21
	s_addc_u32 s5, s47, s20
	s_mul_i32 s6, s19, 0xe00000
	s_add_u32 s6, s50, s6
	s_addc_u32 s7, s51, 0
	s_add_u32 s80, s6, 0x27200000
	s_addc_u32 s81, s7, 0
	s_mov_b64 s[6:7], 0
	s_branch .LBB0_740

.LBB0_790:
	s_cmp_ge_u32 s17, s16
	v_mov_b32_e32 v66, 0x1690
	s_cbranch_scc1 .LBB0_794
	s_waitcnt vmcnt(0)
	v_add_u32_e32 v66, 0x680, v230
	s_add_i32 s11, s17, 1
	s_cmp_ge_u32 s11, s16
	s_cbranch_scc1 .LBB0_794
	v_cmp_gt_i32_e32 vcc, 0x1690, v66
	s_and_saveexec_b64 s[28:29], vcc
	s_cbranch_execz .Lpcl_2
	v_mov_b32_e32 v231, 0
	v_mov_b32_e32 v230, 1
	global_atomic_add v230, v231, v230, s[50:51] offset:1280 sc0
.Lpcl_2:
	s_or_b64 exec, exec, s[28:29]
.LBB0_794:
	v_mov_b32_e32 v67, s65
	ds_write_b32 v67, v66

.LBB0_1022:
	s_or_b64 exec, exec, s[4:5]
	s_waitcnt vmcnt(0)
	v_readfirstlane_b32 s4, v3
	s_nop 1
	v_add_u32_e32 v2, s4, v2
	s_add_i32 s4, 0, 0x20180
	v_add_u32_e32 v2, 0x680, v2
	v_mov_b32_e32 v3, s4
	ds_write_b32 v3, v2
	v_cmp_gt_i32_e32 vcc, 0x1690, v2
	s_and_saveexec_b64 s[4:5], vcc
	s_cbranch_execz .Lpcp_3
	v_mov_b32_e32 v231, 0
	v_mov_b32_e32 v230, 1
	global_atomic_add v230, v231, v230, s[30:31] offset:1280 sc0
.Lpcp_3:
	s_or_b64 exec, exec, s[4:5]
.LBB0_1023:
	s_or_b64 exec, exec, s[2:3]
	s_add_i32 s2, 0, 0x20180
	v_mov_b32_e32 v2, s2
	s_waitcnt lgkmcnt(0)
	s_waitcnt lgkmcnt(0)
	s_barrier
	ds_read_b32 v2, v2
	s_movk_i32 s3, 0x168f
	s_movk_i32 s2, 0x1690
	s_waitcnt lgkmcnt(0)
	v_cmp_lt_i32_e32 vcc, s3, v2
	v_readfirstlane_b32 s11, v2
	v_cmp_gt_i32_e64 s[2:3], s2, v2
	s_cbranch_vccnz .LBB0_1029
	s_cmpk_gt_i32 s11, 0x67f
	s_cbranch_scc0 .LBB0_1030
	s_cmpk_gt_u32 s11, 0xa9f
	s_cbranch_scc0 .LBB0_1031
	s_add_i32 s4, s11, 0xfffff560
	s_bfe_u32 s5, s4, 0x100007
	s_mulk_i32 s5, 0x2493
	s_lshr_b32 s13, s5, 16
	s_mul_i32 s12, s13, 0xfffffc80
	s_add_i32 s12, s12, s4
	s_cmpk_gt_i32 s12, 0x1bf
	s_mul_hi_u32 s16, s13, 0x3800000
	s_mul_i32 s17, s13, 0x3800000
	s_cbranch_scc0 .LBB0_1033
	s_cmpk_gt_u32 s12, 0x37f
	s_cbranch_scc0 .LBB0_1034
	s_add_i32 s10, s12, 0xfffffc80
	s_add_u32 s4, s26, s17
	s_addc_u32 s5, s27, s16
	s_mul_i32 s6, s13, 0xe00000
	s_add_u32 s6, s30, s6
	s_addc_u32 s7, s31, 0
	s_add_u32 s80, s6, 0x27200000
	s_addc_u32 s81, s7, 0
	s_mov_b64 s[6:7], 0
	s_branch .LBB0_1035

.LBB0_1084:
	s_cmp_eq_u32 s62, 0
	s_cbranch_scc1 .LBB0_1088
	s_waitcnt vmcnt(0)
	v_add_u32_e32 v66, 0x680, v230
	s_cmp_eq_u32 s62, 1
	s_cbranch_scc1 .LBB0_1089
	v_cmp_gt_i32_e32 vcc, 0x1690, v66
	s_and_saveexec_b64 s[28:29], vcc
	s_cbranch_execz .Lpcl_3
	v_mov_b32_e32 v231, 0
	v_mov_b32_e32 v230, 1
	global_atomic_add v230, v231, v230, s[50:51] offset:1280 sc0

.LBB0_1511:
	s_or_b64 exec, exec, s[12:13]
	s_waitcnt vmcnt(0)
	v_readfirstlane_b32 s10, v3
	s_nop 1
	v_add_u32_e32 v2, s10, v2
	s_add_i32 s10, 0, 0x20180
	v_add_u32_e32 v2, 0x340, v2
	v_mov_b32_e32 v3, s10
	ds_write_b32 v3, v2
	v_cmp_gt_i32_e32 vcc, 0x680, v2
	s_and_saveexec_b64 s[12:13], vcc
	s_cbranch_execz .Lpcp_4
	v_mov_b32_e32 v231, 0
	v_mov_b32_e32 v230, 1
	global_atomic_add v230, v231, v230, s[50:51] offset:1024 sc0
.Lpcp_4:
	s_or_b64 exec, exec, s[12:13]
.LBB0_1512:
	s_or_b64 exec, exec, s[2:3]
	s_add_i32 s2, 0, 0x20180
	s_waitcnt vmcnt(15)
	v_mov_b32_e32 v2, s2
	s_waitcnt lgkmcnt(0)
	s_waitcnt lgkmcnt(0)
	s_barrier
	ds_read_b32 v2, v2
	s_movk_i32 s3, 0x67f
	s_movk_i32 s2, 0x680
	s_waitcnt lgkmcnt(0)
	v_cmp_lt_i32_e32 vcc, s3, v2
	v_readfirstlane_b32 s11, v2
	v_cmp_gt_i32_e64 s[2:3], s2, v2
	s_cbranch_vccnz .LBB0_1517
	s_cmpk_gt_i32 s11, 0x67f
	s_cbranch_scc0 .LBB0_1518
	s_cmpk_gt_u32 s11, 0xa9f
	s_cbranch_scc0 .LBB0_1519
	s_add_i32 s16, s11, 0xfffff560
	s_cmpk_gt_u32 s16, 0x1bf
	s_cbranch_scc0 .LBB0_1521
	s_add_i32 s10, s11, 0xfffff3a0
	s_add_u32 s86, s50, 0xb200000
	s_addc_u32 s87, s51, 0
	s_mov_b64 s[28:29], 0
	s_mov_b64 s[12:13], s[44:45]
	s_branch .LBB0_1522

.LBB0_1565:
	s_cmp_ge_u32 s16, s17
	v_mov_b32_e32 v66, 0x680
	s_cbranch_scc1 .LBB0_1569
	s_waitcnt vmcnt(0)
	v_add_u32_e32 v66, 0x340, v230
	s_add_i32 s6, s16, 1
	s_cmp_ge_u32 s6, s17
	s_cbranch_scc1 .LBB0_1569
	v_cmp_gt_i32_e32 vcc, 0x680, v66
	s_and_saveexec_b64 s[28:29], vcc
	s_cbranch_execz .Lpcl_4
	v_mov_b32_e32 v231, 0
	v_mov_b32_e32 v230, 1
	v_readlane_b32 s36, v254, 38
	v_readlane_b32 s50, v254, 52
	v_readlane_b32 s51, v254, 53
	v_readlane_b32 s37, v254, 39
	v_readlane_b32 s38, v254, 40
	v_readlane_b32 s39, v254, 41
	v_readlane_b32 s40, v254, 42
	v_readlane_b32 s41, v254, 43
	global_atomic_add v230, v231, v230, s[50:51] offset:1024 sc0
	v_readlane_b32 s42, v254, 44
	v_readlane_b32 s43, v254, 45
	v_readlane_b32 s44, v254, 46
	v_readlane_b32 s45, v254, 47
	v_readlane_b32 s46, v254, 48
	v_readlane_b32 s47, v254, 49
	v_readlane_b32 s48, v254, 50
	v_readlane_b32 s49, v254, 51
.Lpcl_4:
	s_or_b64 exec, exec, s[28:29]
.LBB0_1569:
	v_mov_b32_e32 v67, s25
	ds_write_b32 v67, v66

.LBB0_2054:
	s_or_b64 exec, exec, s[6:7]
	s_waitcnt vmcnt(0)
	v_readfirstlane_b32 s6, v3
	s_nop 1
	v_add_u32_e32 v2, s6, v2
	s_add_i32 s6, 0, 0x20180
	v_add_u32_e32 v2, 0x1690, v2
	v_mov_b32_e32 v3, s6
	ds_write_b32 v3, v2
	v_cmp_gt_i32_e32 vcc, 0x26a0, v2
	s_and_saveexec_b64 s[6:7], vcc
	s_cbranch_execz .Lpcp_5
	v_mov_b32_e32 v231, 0
	v_mov_b32_e32 v230, 1
	global_atomic_add v230, v231, v230, s[50:51] offset:1536 sc0
.Lpcp_5:
	s_or_b64 exec, exec, s[6:7]
.LBB0_2055:
	s_or_b64 exec, exec, s[2:3]
	s_add_i32 s2, 0, 0x20180
	v_mov_b32_e32 v2, s2
	s_waitcnt lgkmcnt(0)
	s_waitcnt lgkmcnt(0)
	s_barrier
	ds_read_b32 v2, v2
	s_movk_i32 s3, 0x269f
	s_movk_i32 s2, 0x26a0
	s_waitcnt lgkmcnt(0)
	v_cmp_lt_i32_e32 vcc, s3, v2
	v_readfirstlane_b32 s11, v2
	v_cmp_gt_i32_e64 s[2:3], s2, v2
	s_cbranch_vccnz .LBB0_2061
	s_cmpk_gt_i32 s11, 0x67f
	s_cbranch_scc0 .LBB0_2062
	s_cmpk_gt_u32 s11, 0xa9f
	s_cbranch_scc0 .LBB0_2063
	s_add_i32 s6, s11, 0xfffff560
	s_bfe_u32 s7, s6, 0x100007
	s_mulk_i32 s7, 0x2493
	s_lshr_b32 s18, s7, 16
	s_mul_i32 s17, s18, 0xfffffc80
	s_add_i32 s17, s17, s6
	s_cmpk_gt_i32 s17, 0x1bf
	s_mul_hi_u32 s19, s18, 0x3800000
	s_mul_i32 s25, s18, 0x3800000
	s_cbranch_scc0 .LBB0_2064
	s_cmpk_gt_u32 s17, 0x37f
	s_cbranch_scc0 .LBB0_2065
	s_add_i32 s10, s17, 0xfffffc80
	s_add_u32 s6, s46, s25
	s_addc_u32 s7, s47, s19
	s_mul_i32 s20, s18, 0xe00000
	s_add_u32 s20, s50, s20
	s_addc_u32 s21, s51, 0
	s_add_u32 s78, s20, 0x27200000
	s_addc_u32 s79, s21, 0
	s_mov_b64 s[20:21], 0
	s_branch .LBB0_2066

.LBB0_2117:
	s_cmp_gt_u32 s17, 20
	v_mov_b32_e32 v66, 0x26a0
	s_cbranch_scc1 .LBB0_2121
	s_waitcnt vmcnt(0)
	v_add_u32_e32 v66, 0x1690, v230
	s_cmp_gt_u32 s17, 19
	s_cbranch_scc1 .LBB0_2121
	v_cmp_gt_i32_e32 vcc, 0x26a0, v66
	s_and_saveexec_b64 s[28:29], vcc
	s_cbranch_execz .Lpcl_5
	v_mov_b32_e32 v231, 0
	v_mov_b32_e32 v230, 1
	v_readlane_b32 s36, v254, 38
	v_readlane_b32 s50, v254, 52
	v_readlane_b32 s51, v254, 53
	v_readlane_b32 s37, v254, 39
	v_readlane_b32 s38, v254, 40
	v_readlane_b32 s39, v254, 41
	v_readlane_b32 s40, v254, 42
	v_readlane_b32 s41, v254, 43
	global_atomic_add v230, v231, v230, s[50:51] offset:1536 sc0
	v_readlane_b32 s42, v254, 44
	v_readlane_b32 s43, v254, 45
	v_readlane_b32 s44, v254, 46
	v_readlane_b32 s45, v254, 47
	v_readlane_b32 s46, v254, 48
	v_readlane_b32 s47, v254, 49
	v_readlane_b32 s48, v254, 50
	v_readlane_b32 s49, v254, 51
.Lpcl_5:
	s_or_b64 exec, exec, s[28:29]
.LBB0_2121:
	v_mov_b32_e32 v67, s82
	ds_write_b32 v67, v66

.LBB0_2296:
	s_or_b64 exec, exec, s[4:5]
	s_waitcnt vmcnt(0)
	v_readfirstlane_b32 s4, v3
	s_nop 1
	v_add_u32_e32 v2, s4, v2
	s_add_i32 s4, 0, 0x20180
	v_add_u32_e32 v2, 0x1690, v2
	v_mov_b32_e32 v3, s4
	ds_write_b32 v3, v2
	v_cmp_gt_i32_e32 vcc, 0x26a0, v2
	s_and_saveexec_b64 s[4:5], vcc
	s_cbranch_execz .Lpcp_6
	v_mov_b32_e32 v231, 0
	v_mov_b32_e32 v230, 1
	global_atomic_add v230, v231, v230, s[94:95] offset:1536 sc0
.Lpcp_6:
	s_or_b64 exec, exec, s[4:5]
.LBB0_2297:
	s_or_b64 exec, exec, s[2:3]
	s_add_i32 s2, 0, 0x20180
	s_waitcnt vmcnt(15)
	v_mov_b32_e32 v2, s2
	s_waitcnt lgkmcnt(0)
	s_waitcnt lgkmcnt(0)
	s_barrier
	ds_read_b32 v2, v2
	s_movk_i32 s3, 0x269f
	s_movk_i32 s2, 0x26a0
	s_waitcnt lgkmcnt(0)
	v_cmp_lt_i32_e32 vcc, s3, v2
	v_readfirstlane_b32 s11, v2
	v_cmp_gt_i32_e64 s[2:3], s2, v2
	s_cbranch_vccnz .LBB0_2303
	s_cmpk_gt_i32 s11, 0x67f
	s_cbranch_scc0 .LBB0_2304
	s_cmpk_gt_u32 s11, 0xa9f
	s_cbranch_scc0 .LBB0_2305
	s_add_i32 s4, s11, 0xfffff560
	s_bfe_u32 s5, s4, 0x100007
	s_mulk_i32 s5, 0x2493
	s_lshr_b32 s19, s5, 16
	s_mul_i32 s18, s19, 0xfffffc80
	s_add_i32 s18, s18, s4
	s_cmpk_gt_i32 s18, 0x1bf
	s_mul_hi_u32 s20, s19, 0x3800000
	s_mul_i32 s21, s19, 0x3800000
	s_cbranch_scc0 .LBB0_2306
	s_cmpk_gt_u32 s18, 0x37f
	s_cbranch_scc0 .LBB0_2307
	s_add_i32 s10, s18, 0xfffffc80
	s_add_u32 s4, s90, s21
	s_addc_u32 s5, s91, s20
	s_mul_i32 s6, s19, 0xe00000
	s_add_u32 s6, s94, s6
	s_addc_u32 s7, s95, 0
	s_add_u32 s52, s6, 0x27200000
	s_addc_u32 s53, s7, 0
	s_mov_b64 s[6:7], 0
	s_branch .LBB0_2308

.LBB0_2358:
	s_cmp_ge_u32 s17, s33
	v_mov_b32_e32 v66, 0x26a0
	s_cbranch_scc1 .LBB0_2362
	s_waitcnt vmcnt(0)
	v_add_u32_e32 v66, 0x1690, v230
	s_add_i32 s18, s17, 1
	s_cmp_ge_u32 s18, s33
	s_cbranch_scc1 .LBB0_2362
	v_cmp_gt_i32_e32 vcc, 0x26a0, v66
	s_and_saveexec_b64 s[28:29], vcc
	s_cbranch_execz .Lpcl_6
	v_mov_b32_e32 v231, 0
	v_mov_b32_e32 v230, 1
	global_atomic_add v230, v231, v230, s[94:95] offset:1536 sc0
.Lpcl_6:
	s_or_b64 exec, exec, s[28:29]
.LBB0_2362:
	v_mov_b32_e32 v67, s71
	ds_write_b32 v67, v66

.Lpcp_7:
	s_or_b64 exec, exec, s[4:5]
.LBB0_2591:
	s_or_b64 exec, exec, s[2:3]
	s_add_i32 s2, 0, 0x20180
	v_mov_b32_e32 v2, s2
	s_waitcnt lgkmcnt(0)
	s_waitcnt lgkmcnt(0)
	s_barrier
	ds_read_b32 v2, v2
	s_movk_i32 s3, 0x269f
	s_movk_i32 s2, 0x26a0
	s_waitcnt lgkmcnt(0)
	v_cmp_lt_i32_e32 vcc, s3, v2
	v_readfirstlane_b32 s11, v2
	v_cmp_gt_i32_e64 s[2:3], s2, v2
	s_cbranch_vccnz .LBB0_2597
	s_cmpk_gt_i32 s11, 0x67f
	s_cbranch_scc0 .LBB0_2598
	s_cmpk_gt_u32 s11, 0xa9f
	s_cbranch_scc0 .LBB0_2599
	s_add_i32 s4, s11, 0xfffff560
	s_bfe_u32 s5, s4, 0x100007
	s_mulk_i32 s5, 0x2493
	s_lshr_b32 s19, s5, 16
	s_mul_i32 s18, s19, 0xfffffc80
	s_add_i32 s18, s18, s4
	s_cmpk_gt_i32 s18, 0x1bf
	s_mul_hi_u32 s20, s19, 0x3800000
	s_mul_i32 s21, s19, 0x3800000
	s_cbranch_scc0 .LBB0_2601
	s_cmpk_gt_u32 s18, 0x37f
	s_cbranch_scc0 .LBB0_2602
	s_add_i32 s10, s18, 0xfffffc80
	s_add_u32 s4, s90, s21
	s_addc_u32 s5, s91, s20
	s_mul_i32 s6, s19, 0xe00000
	s_add_u32 s6, s94, s6
	s_addc_u32 s7, s95, 0
	s_add_u32 s52, s6, 0x27200000
	s_addc_u32 s53, s7, 0
	s_mov_b64 s[6:7], 0
	s_branch .LBB0_2603

.LBB0_2652:
	s_cmp_eq_u32 s68, 0
	s_cbranch_scc1 .LBB0_2656
	s_waitcnt vmcnt(0)
	v_add_u32_e32 v66, 0x1690, v230
	s_cmp_eq_u32 s68, 1
	s_cbranch_scc1 .LBB0_2657
	v_cmp_gt_i32_e32 vcc, 0x26a0, v66
	s_and_saveexec_b64 s[28:29], vcc
	s_cbranch_execz .Lpcl_7
	v_mov_b32_e32 v231, 0
	v_mov_b32_e32 v230, 1
	global_atomic_add v230, v231, v230, s[94:95] offset:1536 sc0

.LBB0_3130:
	s_or_b64 exec, exec, s[6:7]
	s_waitcnt vmcnt(0)
	v_readfirstlane_b32 s6, v2
	s_nop 1
	v_add_u32_e32 v1, s6, v1
	s_add_i32 s6, 0, 0x20180
	v_add_u32_e32 v1, 0x26a0, v1
	v_mov_b32_e32 v2, s6
	ds_write_b32 v2, v1
	v_cmp_gt_i32_e32 vcc, 0x34a0, v1
	s_and_saveexec_b64 s[6:7], vcc
	s_cbranch_execz .Lpcp_8
	v_mov_b32_e32 v231, 0
	v_mov_b32_e32 v230, 1
	global_atomic_add v230, v231, v230, s[94:95] offset:2048 sc0
.Lpcp_8:
	s_or_b64 exec, exec, s[6:7]
.LBB0_3131:
	s_or_b64 exec, exec, s[2:3]
	s_add_i32 s2, 0, 0x20180
	v_mov_b32_e32 v1, s2
	s_waitcnt lgkmcnt(0)
	s_waitcnt lgkmcnt(0)
	s_barrier
	ds_read_b32 v1, v1
	s_movk_i32 s3, 0x349f
	s_movk_i32 s2, 0x34a0
	s_waitcnt lgkmcnt(0)
	v_cmp_lt_i32_e32 vcc, s3, v1
	v_readfirstlane_b32 s14, v1
	v_cmp_gt_i32_e64 s[2:3], s2, v1
	s_cbranch_vccnz .LBB0_3136
	s_cmpk_gt_i32 s14, 0x67f
	s_cbranch_scc0 .LBB0_3137
	s_cmpk_gt_u32 s14, 0xa9f
	s_cbranch_scc0 .LBB0_3138
	s_cmpk_gt_u32 s14, 0x269f
	s_cbranch_scc0 .LBB0_3139
	s_add_i32 s6, s14, 0xd960
	s_bfe_u32 s6, s6, 0xa0006
	s_mulk_i32 s6, 0x2493
	s_lshr_b32 s17, s6, 16
	s_mul_i32 s6, s17, 0xfffffe40
	s_add_i32 s6, s14, s6
	s_add_i32 s15, s6, 0xffffdce0
	s_mov_b64 s[6:7], 0
	s_branch .LBB0_3140

.LBB0_3196:
	s_cmp_eq_u32 s59, 0
	s_cbranch_scc1 .LBB0_3200
	s_waitcnt vmcnt(0)
	v_add_u32_e32 v66, 0x26a0, v230
	s_cmp_eq_u32 s59, 1
	s_cbranch_scc1 .LBB0_3201
	v_cmp_gt_i32_e32 vcc, 0x34a0, v66
	s_and_saveexec_b64 s[20:21], vcc
	s_cbranch_execz .Lpcl_8
	v_mov_b32_e32 v231, 0
	v_mov_b32_e32 v230, 1
	global_atomic_add v230, v231, v230, s[94:95] offset:2048 sc0
.Lpcl_8:
	s_or_b64 exec, exec, s[20:21]
	s_branch .LBB0_3201

.LBB0_3372:
	s_or_b64 exec, exec, s[4:5]
	s_waitcnt vmcnt(0)
	v_readfirstlane_b32 s4, v2
	s_nop 1
	v_add_u32_e32 v1, s4, v1
	s_add_i32 s4, 0, 0x20180
	v_add_u32_e32 v1, 0x26a0, v1
	v_mov_b32_e32 v2, s4
	ds_write_b32 v2, v1
	v_cmp_gt_i32_e32 vcc, 0x34a0, v1
	s_and_saveexec_b64 s[4:5], vcc
	s_cbranch_execz .Lpcp_9
	v_mov_b32_e32 v231, 0
	v_mov_b32_e32 v230, 1
	global_atomic_add v230, v231, v230, s[94:95] offset:2048 sc0
.Lpcp_9:
	s_or_b64 exec, exec, s[4:5]
.LBB0_3373:
	s_or_b64 exec, exec, s[2:3]
	s_add_i32 s2, 0, 0x20180
	v_mov_b32_e32 v1, s2
	s_waitcnt lgkmcnt(0)
	s_waitcnt lgkmcnt(0)
	s_barrier
	ds_read_b32 v1, v1
	s_movk_i32 s3, 0x349f
	s_movk_i32 s2, 0x34a0
	s_waitcnt lgkmcnt(0)
	v_cmp_lt_i32_e32 vcc, s3, v1
	v_readfirstlane_b32 s12, v1
	v_cmp_gt_i32_e64 s[2:3], s2, v1
	s_cbranch_vccnz .LBB0_3378
	s_cmpk_gt_i32 s12, 0x67f
	s_cbranch_scc0 .LBB0_3379
	s_cmpk_gt_u32 s12, 0xa9f
	s_cbranch_scc0 .LBB0_3380
	s_cmpk_gt_u32 s12, 0x269f
	s_cbranch_scc0 .LBB0_3381
	s_add_i32 s4, s12, 0xd960
	s_bfe_u32 s4, s4, 0xa0006
	s_mulk_i32 s4, 0x2493
	s_lshr_b32 s15, s4, 16
	s_mul_i32 s4, s15, 0xfffffe40
	s_add_i32 s4, s12, s4
	s_add_i32 s13, s4, 0xffffdce0
	s_mov_b64 s[4:5], 0
	s_branch .LBB0_3382

.LBB0_3438:
	s_cmp_eq_u32 s54, 0
	s_cbranch_scc1 .LBB0_3442
	s_waitcnt vmcnt(0)
	v_add_u32_e32 v66, 0x26a0, v230
	s_cmp_eq_u32 s54, 1
	s_cbranch_scc1 .LBB0_3443
	v_cmp_gt_i32_e32 vcc, 0x34a0, v66
	s_and_saveexec_b64 s[18:19], vcc
	s_cbranch_execz .Lpcl_9
	v_mov_b32_e32 v231, 0
	v_mov_b32_e32 v230, 1
	global_atomic_add v230, v231, v230, s[94:95] offset:2048 sc0
.Lpcl_9:
	s_or_b64 exec, exec, s[18:19]
	s_branch .LBB0_3443
